# loop-edge rotation: proj, out and MoE1 K-loops close with one conditional back-branch (s_cselect + s_cbranch_scc0); downstream code placement kept
# speedup vs baseline: 1.0114x; 1.0017x over previous
.LBB0_500:
	s_and_b64 s[30:31], s[24:25], s[28:29]
	s_add_i32 s23, s5, 2
	s_and_b64 s[28:29], s[28:29], exec
	s_cselect_b32 s96, 0, s23
	s_and_b64 s[28:29], s[30:31], exec
	s_cselect_b32 s28, s52, s4
	s_ashr_i32 s29, s28, 31
	s_lshl_b64 s[30:31], s[96:97], 7
	s_or_b32 s96, s96, 1
	s_lshl_b64 s[34:35], s[28:29], 18
	s_lshl_b64 s[28:29], s[96:97], 7
	s_add_u32 s72, s6, s34
	s_addc_u32 s73, s7, s35
	s_add_u32 s34, s72, s30
	s_addc_u32 s35, s73, s31
	s_mov_b32 m0, s56
	ds_read_b128 v[56:59], v239 offset:16384
	ds_read_b128 v[60:63], v240 offset:16384
	ds_read_b128 v[48:51], v239 offset:18432
	ds_read_b128 v[52:55], v240 offset:18432
	ds_read_b128 v[40:43], v239 offset:20480
	ds_read_b128 v[44:47], v240 offset:20480
	ds_read_b128 v[32:35], v239 offset:22528
	ds_read_b128 v[36:39], v240 offset:22528
	global_load_lds_dwordx4 v194, s[34:35]
	s_mov_b32 m0, s57
	s_nop 0
	global_load_lds_dwordx4 v196, s[34:35]
	s_add_u32 s34, s34, 0x20000
	s_addc_u32 s35, s35, 0
	s_mov_b32 m0, s58
	s_add_u32 s30, s78, s30
	global_load_lds_dwordx4 v194, s[34:35]
	s_mov_b32 m0, s59
	s_addc_u32 s31, s79, s31
	global_load_lds_dwordx4 v196, s[34:35]
	s_mov_b32 m0, s49
	s_nop 0
	global_load_lds_dwordx4 v202, s[30:31]
	s_mov_b32 m0, s60
	s_nop 0
	global_load_lds_dwordx4 v204, s[30:31]
	s_waitcnt vmcnt(8)
	s_waitcnt lgkmcnt(0)
	s_barrier
	s_setprio 1
	s_waitcnt lgkmcnt(0)
	v_mfma_scale_f32_16x16x128_f8f6f4 v[126:129], v[8:15], v[56:63], v[126:129], v226, v225 op_sel_hi:[0,0,0]
	v_mfma_scale_f32_16x16x128_f8f6f4 v[122:125], v[24:31], v[56:63], v[122:125], v226, v225 op_sel_hi:[0,0,0]
	v_mfma_scale_f32_16x16x128_f8f6f4 v[110:113], v[8:15], v[48:55], v[110:113], v226, v225 op_sel_hi:[0,0,0]
	v_mfma_scale_f32_16x16x128_f8f6f4 v[106:109], v[24:31], v[48:55], v[106:109], v226, v225 op_sel_hi:[0,0,0]
	v_mfma_scale_f32_16x16x128_f8f6f4 v[92:95], v[8:15], v[40:47], v[92:95], v226, v225 op_sel_hi:[0,0,0]
	v_mfma_scale_f32_16x16x128_f8f6f4 v[88:91], v[24:31], v[40:47], v[88:91], v226, v225 op_sel_hi:[0,0,0]
	v_mfma_scale_f32_16x16x128_f8f6f4 v[76:79], v[8:15], v[32:39], v[76:79], v226, v225 op_sel_hi:[0,0,0]
	v_mfma_scale_f32_16x16x128_f8f6f4 v[72:75], v[24:31], v[32:39], v[72:75], v226, v225 op_sel_hi:[0,0,0]
	s_setprio 0
	s_setprio 1
	v_mfma_scale_f32_16x16x128_f8f6f4 v[118:121], v[0:7], v[56:63], v[118:121], v226, v225 op_sel_hi:[0,0,0]
	v_mfma_scale_f32_16x16x128_f8f6f4 v[114:117], v[16:23], v[56:63], v[114:117], v226, v225 op_sel_hi:[0,0,0]
	v_mfma_scale_f32_16x16x128_f8f6f4 v[102:105], v[0:7], v[48:55], v[102:105], v226, v225 op_sel_hi:[0,0,0]
	v_mfma_scale_f32_16x16x128_f8f6f4 v[98:101], v[16:23], v[48:55], v[98:101], v226, v225 op_sel_hi:[0,0,0]
	v_mfma_scale_f32_16x16x128_f8f6f4 v[84:87], v[0:7], v[40:47], v[84:87], v226, v225 op_sel_hi:[0,0,0]
	v_mfma_scale_f32_16x16x128_f8f6f4 v[80:83], v[16:23], v[40:47], v[80:83], v226, v225 op_sel_hi:[0,0,0]
	v_mfma_scale_f32_16x16x128_f8f6f4 v[68:71], v[0:7], v[32:39], v[68:71], v226, v225 op_sel_hi:[0,0,0]
	v_mfma_scale_f32_16x16x128_f8f6f4 v[64:67], v[16:23], v[32:39], v[64:67], v226, v225 op_sel_hi:[0,0,0]
	s_setprio 0
	s_barrier
	s_add_i32 s34, 0, 0x18000
	s_add_i32 s35, 0, 0x1c000
	ds_read_b128 v[0:3], v205 offset:32768
	ds_read_b128 v[4:7], v237 offset:32768
	ds_read_b128 v[8:11], v205 offset:34816
	ds_read_b128 v[12:15], v237 offset:34816
	ds_read_b128 v[16:19], v205 offset:49152
	ds_read_b128 v[20:23], v237 offset:49152
	ds_read_b128 v[24:27], v205 offset:51200
	ds_read_b128 v[28:31], v237 offset:51200
	s_mov_b32 m0, s61
	ds_read_b128 v[32:35], v239 offset:32768
	ds_read_b128 v[40:43], v239 offset:34816
	ds_read_b128 v[36:39], v240 offset:32768
	ds_read_b128 v[44:47], v240 offset:34816
	ds_read_b128 v[48:51], v239 offset:36864
	ds_read_b128 v[56:59], v239 offset:38912
	ds_read_b128 v[52:55], v240 offset:36864
	ds_read_b128 v[60:63], v240 offset:38912
	global_load_lds_dwordx4 v214, s[30:31]
	s_mov_b32 m0, s64
	s_nop 0
	global_load_lds_dwordx4 v212, s[30:31]
	s_waitcnt vmcnt(8)
	s_waitcnt lgkmcnt(0)
	s_barrier
	s_setprio 1
	s_waitcnt lgkmcnt(0)
	v_mfma_scale_f32_16x16x128_f8f6f4 v[190:193], v[0:7], v[32:39], v[190:193], v226, v225 op_sel_hi:[0,0,0]
	v_mfma_scale_f32_16x16x128_f8f6f4 v[186:189], v[8:15], v[32:39], v[186:189], v226, v225 op_sel_hi:[0,0,0]
	v_mfma_scale_f32_16x16x128_f8f6f4 v[174:177], v[0:7], v[40:47], v[174:177], v226, v225 op_sel_hi:[0,0,0]
	v_mfma_scale_f32_16x16x128_f8f6f4 v[170:173], v[8:15], v[40:47], v[170:173], v226, v225 op_sel_hi:[0,0,0]
	v_mfma_scale_f32_16x16x128_f8f6f4 v[158:161], v[0:7], v[48:55], v[158:161], v226, v225 op_sel_hi:[0,0,0]
	v_mfma_scale_f32_16x16x128_f8f6f4 v[154:157], v[8:15], v[48:55], v[154:157], v226, v225 op_sel_hi:[0,0,0]
	v_mfma_scale_f32_16x16x128_f8f6f4 v[142:145], v[0:7], v[56:63], v[142:145], v226, v225 op_sel_hi:[0,0,0]
	v_mfma_scale_f32_16x16x128_f8f6f4 v[138:141], v[8:15], v[56:63], v[138:141], v226, v225 op_sel_hi:[0,0,0]
	s_setprio 0
	s_setprio 1
	v_mfma_scale_f32_16x16x128_f8f6f4 v[182:185], v[16:23], v[32:39], v[182:185], v226, v225 op_sel_hi:[0,0,0]
	v_mfma_scale_f32_16x16x128_f8f6f4 v[178:181], v[24:31], v[32:39], v[178:181], v226, v225 op_sel_hi:[0,0,0]
	v_mfma_scale_f32_16x16x128_f8f6f4 v[166:169], v[16:23], v[40:47], v[166:169], v226, v225 op_sel_hi:[0,0,0]
	v_mfma_scale_f32_16x16x128_f8f6f4 v[162:165], v[24:31], v[40:47], v[162:165], v226, v225 op_sel_hi:[0,0,0]
	v_mfma_scale_f32_16x16x128_f8f6f4 v[150:153], v[16:23], v[48:55], v[150:153], v226, v225 op_sel_hi:[0,0,0]
	v_mfma_scale_f32_16x16x128_f8f6f4 v[146:149], v[24:31], v[48:55], v[146:149], v226, v225 op_sel_hi:[0,0,0]
	v_mfma_scale_f32_16x16x128_f8f6f4 v[134:137], v[16:23], v[56:63], v[134:137], v226, v225 op_sel_hi:[0,0,0]
	v_mfma_scale_f32_16x16x128_f8f6f4 v[130:133], v[24:31], v[56:63], v[130:133], v226, v225 op_sel_hi:[0,0,0]
	s_setprio 0
	s_barrier
	s_add_u32 s30, s72, s28
	s_addc_u32 s31, s73, s29
	s_add_i32 s34, s34, s48
	s_mov_b32 m0, s34
	ds_read_b128 v[32:35], v239 offset:49152
	ds_read_b128 v[40:43], v239 offset:51200
	ds_read_b128 v[36:39], v240 offset:49152
	ds_read_b128 v[44:47], v240 offset:51200
	ds_read_b128 v[48:51], v239 offset:53248
	ds_read_b128 v[56:59], v239 offset:55296
	ds_read_b128 v[52:55], v240 offset:53248
	ds_read_b128 v[60:63], v240 offset:55296
	global_load_lds_dwordx4 v194, s[30:31]
	s_add_i32 m0, s34, 0x2000
	s_add_i32 s34, s35, s48
	global_load_lds_dwordx4 v196, s[30:31]
	s_add_u32 s30, s30, 0x20000
	s_addc_u32 s31, s31, 0
	s_mov_b32 m0, s34
	s_nop 0
	global_load_lds_dwordx4 v194, s[30:31]
	s_add_i32 m0, s34, 0x2000
	s_add_u32 s28, s78, s28
	global_load_lds_dwordx4 v196, s[30:31]
	s_addc_u32 s29, s79, s29
	s_mov_b32 m0, s65
	s_nop 0
	global_load_lds_dwordx4 v202, s[28:29]
	s_mov_b32 m0, s92
	s_nop 0
	global_load_lds_dwordx4 v204, s[28:29]
	s_waitcnt vmcnt(8)
	s_waitcnt lgkmcnt(0)
	s_barrier
	s_setprio 1
	s_waitcnt lgkmcnt(0)
	v_mfma_scale_f32_16x16x128_f8f6f4 v[126:129], v[0:7], v[32:39], v[126:129], v226, v225 op_sel_hi:[0,0,0]
	v_mfma_scale_f32_16x16x128_f8f6f4 v[122:125], v[8:15], v[32:39], v[122:125], v226, v225 op_sel_hi:[0,0,0]
	v_mfma_scale_f32_16x16x128_f8f6f4 v[110:113], v[0:7], v[40:47], v[110:113], v226, v225 op_sel_hi:[0,0,0]
	v_mfma_scale_f32_16x16x128_f8f6f4 v[106:109], v[8:15], v[40:47], v[106:109], v226, v225 op_sel_hi:[0,0,0]
	v_mfma_scale_f32_16x16x128_f8f6f4 v[92:95], v[0:7], v[48:55], v[92:95], v226, v225 op_sel_hi:[0,0,0]
	v_mfma_scale_f32_16x16x128_f8f6f4 v[88:91], v[8:15], v[48:55], v[88:91], v226, v225 op_sel_hi:[0,0,0]
	v_mfma_scale_f32_16x16x128_f8f6f4 v[76:79], v[0:7], v[56:63], v[76:79], v226, v225 op_sel_hi:[0,0,0]
	v_mfma_scale_f32_16x16x128_f8f6f4 v[72:75], v[8:15], v[56:63], v[72:75], v226, v225 op_sel_hi:[0,0,0]
	s_setprio 0
	s_setprio 1
	v_mfma_scale_f32_16x16x128_f8f6f4 v[118:121], v[16:23], v[32:39], v[118:121], v226, v225 op_sel_hi:[0,0,0]
	v_mfma_scale_f32_16x16x128_f8f6f4 v[114:117], v[24:31], v[32:39], v[114:117], v226, v225 op_sel_hi:[0,0,0]
	v_mfma_scale_f32_16x16x128_f8f6f4 v[102:105], v[16:23], v[40:47], v[102:105], v226, v225 op_sel_hi:[0,0,0]
	v_mfma_scale_f32_16x16x128_f8f6f4 v[98:101], v[24:31], v[40:47], v[98:101], v226, v225 op_sel_hi:[0,0,0]
	v_mfma_scale_f32_16x16x128_f8f6f4 v[84:87], v[16:23], v[48:55], v[84:87], v226, v225 op_sel_hi:[0,0,0]
	v_mfma_scale_f32_16x16x128_f8f6f4 v[80:83], v[24:31], v[48:55], v[80:83], v226, v225 op_sel_hi:[0,0,0]
	v_mfma_scale_f32_16x16x128_f8f6f4 v[68:71], v[16:23], v[56:63], v[68:71], v226, v225 op_sel_hi:[0,0,0]
	v_mfma_scale_f32_16x16x128_f8f6f4 v[64:67], v[24:31], v[56:63], v[64:67], v226, v225 op_sel_hi:[0,0,0]
	s_setprio 0
	s_barrier
	s_add_u32 s26, s26, 0x100
	s_addc_u32 s27, s27, 0
	s_cmp_gt_u32 s5, 5
	s_cselect_b32 s5, s5, s23
	s_cbranch_scc0 .LBB0_497
.LBB0_502:
	s_nop 0
	s_and_b64 vcc, exec, s[20:21]
	s_cbranch_vccz .LBB0_504
	s_barrier

.LBB0_989:
	s_and_b64 s[14:15], s[8:9], s[12:13]
	s_add_i32 s52, s49, 2
	s_and_b64 s[12:13], s[12:13], exec
	s_cselect_b32 s96, 0, s52
	s_and_b64 s[12:13], s[14:15], exec
	s_cselect_b32 s12, s47, s23
	s_ashr_i32 s13, s12, 31
	s_lshl_b64 s[14:15], s[96:97], 7
	s_or_b32 s96, s96, 1
	s_lshl_b64 s[16:17], s[12:13], 18
	s_lshl_b64 s[12:13], s[96:97], 7
	s_add_u32 s53, s18, s16
	s_addc_u32 s54, s19, s17
	s_add_u32 s16, s53, s14
	s_addc_u32 s17, s54, s15
	v_lshl_add_u64 v[216:217], s[16:17], 0, v[194:195]
	s_mov_b32 m0, s24
	ds_read_b128 v[56:59], v239 offset:16384
	ds_read_b128 v[60:63], v240 offset:16384
	ds_read_b128 v[48:51], v239 offset:18432
	ds_read_b128 v[52:55], v240 offset:18432
	ds_read_b128 v[40:43], v239 offset:20480
	ds_read_b128 v[44:47], v240 offset:20480
	ds_read_b128 v[32:35], v239 offset:22528
	ds_read_b128 v[36:39], v240 offset:22528
	global_load_lds_dwordx4 v[216:217], off
	v_lshl_add_u64 v[216:217], s[16:17], 0, v[196:197]
	s_add_u32 s16, s16, 0x20000
	s_mov_b32 m0, s25
	s_addc_u32 s17, s17, 0
	global_load_lds_dwordx4 v[216:217], off
	v_lshl_add_u64 v[216:217], s[16:17], 0, v[194:195]
	s_mov_b32 m0, s26
	s_add_u32 s14, s78, s14
	global_load_lds_dwordx4 v[216:217], off
	v_lshl_add_u64 v[216:217], s[16:17], 0, v[196:197]
	s_mov_b32 m0, s27
	s_addc_u32 s15, s79, s15
	global_load_lds_dwordx4 v[216:217], off
	s_mov_b32 m0, s21
	s_nop 0
	global_load_lds_dwordx4 v202, s[14:15]
	s_mov_b32 m0, s28
	s_nop 0
	global_load_lds_dwordx4 v204, s[14:15]
	s_waitcnt vmcnt(8)
	s_waitcnt lgkmcnt(0)
	s_barrier
	s_setprio 1
	s_waitcnt lgkmcnt(0)
	v_mfma_scale_f32_16x16x128_f8f6f4 v[126:129], v[8:15], v[56:63], v[126:129], v226, v225 op_sel_hi:[0,0,0]
	v_mfma_scale_f32_16x16x128_f8f6f4 v[122:125], v[24:31], v[56:63], v[122:125], v226, v225 op_sel_hi:[0,0,0]
	v_mfma_scale_f32_16x16x128_f8f6f4 v[110:113], v[8:15], v[48:55], v[110:113], v226, v225 op_sel_hi:[0,0,0]
	v_mfma_scale_f32_16x16x128_f8f6f4 v[106:109], v[24:31], v[48:55], v[106:109], v226, v225 op_sel_hi:[0,0,0]
	v_mfma_scale_f32_16x16x128_f8f6f4 v[92:95], v[8:15], v[40:47], v[92:95], v226, v225 op_sel_hi:[0,0,0]
	v_mfma_scale_f32_16x16x128_f8f6f4 v[88:91], v[24:31], v[40:47], v[88:91], v226, v225 op_sel_hi:[0,0,0]
	v_mfma_scale_f32_16x16x128_f8f6f4 v[76:79], v[8:15], v[32:39], v[76:79], v226, v225 op_sel_hi:[0,0,0]
	v_mfma_scale_f32_16x16x128_f8f6f4 v[72:75], v[24:31], v[32:39], v[72:75], v226, v225 op_sel_hi:[0,0,0]
	s_setprio 0
	s_setprio 1
	v_mfma_scale_f32_16x16x128_f8f6f4 v[118:121], v[0:7], v[56:63], v[118:121], v226, v225 op_sel_hi:[0,0,0]
	v_mfma_scale_f32_16x16x128_f8f6f4 v[114:117], v[16:23], v[56:63], v[114:117], v226, v225 op_sel_hi:[0,0,0]
	v_mfma_scale_f32_16x16x128_f8f6f4 v[102:105], v[0:7], v[48:55], v[102:105], v226, v225 op_sel_hi:[0,0,0]
	v_mfma_scale_f32_16x16x128_f8f6f4 v[98:101], v[16:23], v[48:55], v[98:101], v226, v225 op_sel_hi:[0,0,0]
	v_mfma_scale_f32_16x16x128_f8f6f4 v[84:87], v[0:7], v[40:47], v[84:87], v226, v225 op_sel_hi:[0,0,0]
	v_mfma_scale_f32_16x16x128_f8f6f4 v[80:83], v[16:23], v[40:47], v[80:83], v226, v225 op_sel_hi:[0,0,0]
	v_mfma_scale_f32_16x16x128_f8f6f4 v[68:71], v[0:7], v[32:39], v[68:71], v226, v225 op_sel_hi:[0,0,0]
	v_mfma_scale_f32_16x16x128_f8f6f4 v[64:67], v[16:23], v[32:39], v[64:67], v226, v225 op_sel_hi:[0,0,0]
	s_setprio 0
	s_barrier
	s_add_i32 s16, 0, 0x18000
	s_add_i32 s17, 0, 0x1c000
	v_add_u32_e32 v0, s16, v205
	v_add_u32_e32 v4, s16, v237
	v_add_u32_e32 v8, s94, v205
	v_add_u32_e32 v12, s94, v237
	v_add_u32_e32 v16, s17, v205
	v_add_u32_e32 v20, s17, v237
	v_add_u32_e32 v24, s33, v205
	v_add_u32_e32 v28, s33, v237
	ds_read_b128 v[0:3], v0
	ds_read_b128 v[4:7], v4
	ds_read_b128 v[8:11], v8
	ds_read_b128 v[12:15], v12
	ds_read_b128 v[16:19], v16
	ds_read_b128 v[20:23], v20
	ds_read_b128 v[24:27], v24
	ds_read_b128 v[28:31], v28
	s_mov_b32 m0, s29
	v_lshl_add_u64 v[214:215], s[14:15], 0, v[214:215]
	ds_read_b128 v[32:35], v239 offset:32768
	ds_read_b128 v[40:43], v239 offset:34816
	ds_read_b128 v[36:39], v240 offset:32768
	ds_read_b128 v[44:47], v240 offset:34816
	ds_read_b128 v[48:51], v239 offset:36864
	ds_read_b128 v[56:59], v239 offset:38912
	ds_read_b128 v[52:55], v240 offset:36864
	ds_read_b128 v[60:63], v240 offset:38912
	global_load_lds_dwordx4 v[214:215], off
	v_lshl_add_u64 v[212:213], s[14:15], 0, v[212:213]
	s_mov_b32 m0, s30
	s_nop 0
	global_load_lds_dwordx4 v[212:213], off
	s_waitcnt vmcnt(8)
	s_waitcnt lgkmcnt(0)
	s_barrier
	s_setprio 1
	s_waitcnt lgkmcnt(0)
	v_mfma_scale_f32_16x16x128_f8f6f4 v[186:189], v[0:7], v[32:39], v[186:189], v226, v225 op_sel_hi:[0,0,0]
	v_mfma_scale_f32_16x16x128_f8f6f4 v[190:193], v[8:15], v[32:39], v[190:193], v226, v225 op_sel_hi:[0,0,0]
	v_mfma_scale_f32_16x16x128_f8f6f4 v[174:177], v[0:7], v[40:47], v[174:177], v226, v225 op_sel_hi:[0,0,0]
	v_mfma_scale_f32_16x16x128_f8f6f4 v[170:173], v[8:15], v[40:47], v[170:173], v226, v225 op_sel_hi:[0,0,0]
	v_mfma_scale_f32_16x16x128_f8f6f4 v[158:161], v[0:7], v[48:55], v[158:161], v226, v225 op_sel_hi:[0,0,0]
	v_mfma_scale_f32_16x16x128_f8f6f4 v[154:157], v[8:15], v[48:55], v[154:157], v226, v225 op_sel_hi:[0,0,0]
	v_mfma_scale_f32_16x16x128_f8f6f4 v[142:145], v[0:7], v[56:63], v[142:145], v226, v225 op_sel_hi:[0,0,0]
	v_mfma_scale_f32_16x16x128_f8f6f4 v[138:141], v[8:15], v[56:63], v[138:141], v226, v225 op_sel_hi:[0,0,0]
	s_setprio 0
	s_setprio 1
	v_mfma_scale_f32_16x16x128_f8f6f4 v[182:185], v[16:23], v[32:39], v[182:185], v226, v225 op_sel_hi:[0,0,0]
	v_mfma_scale_f32_16x16x128_f8f6f4 v[178:181], v[24:31], v[32:39], v[178:181], v226, v225 op_sel_hi:[0,0,0]
	v_mfma_scale_f32_16x16x128_f8f6f4 v[166:169], v[16:23], v[40:47], v[166:169], v226, v225 op_sel_hi:[0,0,0]
	v_mfma_scale_f32_16x16x128_f8f6f4 v[162:165], v[24:31], v[40:47], v[162:165], v226, v225 op_sel_hi:[0,0,0]
	v_mfma_scale_f32_16x16x128_f8f6f4 v[150:153], v[16:23], v[48:55], v[150:153], v226, v225 op_sel_hi:[0,0,0]
	v_mfma_scale_f32_16x16x128_f8f6f4 v[146:149], v[24:31], v[48:55], v[146:149], v226, v225 op_sel_hi:[0,0,0]
	v_mfma_scale_f32_16x16x128_f8f6f4 v[134:137], v[16:23], v[56:63], v[134:137], v226, v225 op_sel_hi:[0,0,0]
	v_mfma_scale_f32_16x16x128_f8f6f4 v[130:133], v[24:31], v[56:63], v[130:133], v226, v225 op_sel_hi:[0,0,0]
	s_setprio 0
	s_barrier
	s_add_u32 s14, s53, s12
	s_addc_u32 s15, s54, s13
	s_add_i32 s16, s16, s20
	v_lshl_add_u64 v[212:213], s[14:15], 0, v[194:195]
	s_mov_b32 m0, s16
	ds_read_b128 v[32:35], v239 offset:49152
	ds_read_b128 v[40:43], v239 offset:51200
	ds_read_b128 v[36:39], v240 offset:49152
	ds_read_b128 v[44:47], v240 offset:51200
	ds_read_b128 v[48:51], v239 offset:53248
	ds_read_b128 v[56:59], v239 offset:55296
	ds_read_b128 v[52:55], v240 offset:53248
	ds_read_b128 v[60:63], v240 offset:55296
	global_load_lds_dwordx4 v[212:213], off
	s_add_i32 m0, s16, 0x2000
	v_lshl_add_u64 v[212:213], s[14:15], 0, v[196:197]
	s_add_u32 s14, s14, 0x20000
	s_addc_u32 s15, s15, 0
	s_add_i32 s16, s17, s20
	global_load_lds_dwordx4 v[212:213], off
	v_lshl_add_u64 v[212:213], s[14:15], 0, v[194:195]
	s_mov_b32 m0, s16
	s_nop 0
	global_load_lds_dwordx4 v[212:213], off
	s_add_i32 m0, s16, 0x2000
	v_lshl_add_u64 v[212:213], s[14:15], 0, v[196:197]
	s_add_u32 s12, s78, s12
	global_load_lds_dwordx4 v[212:213], off
	s_addc_u32 s13, s79, s13
	s_mov_b32 m0, s39
	s_nop 0
	global_load_lds_dwordx4 v202, s[12:13]
	s_mov_b32 m0, s40
	s_nop 0
	global_load_lds_dwordx4 v204, s[12:13]
	s_waitcnt vmcnt(8)
	s_waitcnt lgkmcnt(0)
	s_barrier
	s_setprio 1
	s_waitcnt lgkmcnt(0)
	v_mfma_scale_f32_16x16x128_f8f6f4 v[126:129], v[0:7], v[32:39], v[126:129], v226, v225 op_sel_hi:[0,0,0]
	v_mfma_scale_f32_16x16x128_f8f6f4 v[122:125], v[8:15], v[32:39], v[122:125], v226, v225 op_sel_hi:[0,0,0]
	v_mfma_scale_f32_16x16x128_f8f6f4 v[110:113], v[0:7], v[40:47], v[110:113], v226, v225 op_sel_hi:[0,0,0]
	v_mfma_scale_f32_16x16x128_f8f6f4 v[106:109], v[8:15], v[40:47], v[106:109], v226, v225 op_sel_hi:[0,0,0]
	v_mfma_scale_f32_16x16x128_f8f6f4 v[92:95], v[0:7], v[48:55], v[92:95], v226, v225 op_sel_hi:[0,0,0]
	v_mfma_scale_f32_16x16x128_f8f6f4 v[88:91], v[8:15], v[48:55], v[88:91], v226, v225 op_sel_hi:[0,0,0]
	v_mfma_scale_f32_16x16x128_f8f6f4 v[76:79], v[0:7], v[56:63], v[76:79], v226, v225 op_sel_hi:[0,0,0]
	v_mfma_scale_f32_16x16x128_f8f6f4 v[72:75], v[8:15], v[56:63], v[72:75], v226, v225 op_sel_hi:[0,0,0]
	s_setprio 0
	s_setprio 1
	v_mfma_scale_f32_16x16x128_f8f6f4 v[118:121], v[16:23], v[32:39], v[118:121], v226, v225 op_sel_hi:[0,0,0]
	v_mfma_scale_f32_16x16x128_f8f6f4 v[114:117], v[24:31], v[32:39], v[114:117], v226, v225 op_sel_hi:[0,0,0]
	v_mfma_scale_f32_16x16x128_f8f6f4 v[102:105], v[16:23], v[40:47], v[102:105], v226, v225 op_sel_hi:[0,0,0]
	v_mfma_scale_f32_16x16x128_f8f6f4 v[98:101], v[24:31], v[40:47], v[98:101], v226, v225 op_sel_hi:[0,0,0]
	v_mfma_scale_f32_16x16x128_f8f6f4 v[84:87], v[16:23], v[48:55], v[84:87], v226, v225 op_sel_hi:[0,0,0]
	v_mfma_scale_f32_16x16x128_f8f6f4 v[80:83], v[24:31], v[48:55], v[80:83], v226, v225 op_sel_hi:[0,0,0]
	v_mfma_scale_f32_16x16x128_f8f6f4 v[68:71], v[16:23], v[56:63], v[68:71], v226, v225 op_sel_hi:[0,0,0]
	v_mfma_scale_f32_16x16x128_f8f6f4 v[64:67], v[24:31], v[56:63], v[64:67], v226, v225 op_sel_hi:[0,0,0]
	s_setprio 0
	s_barrier
	s_add_u32 s10, s10, 0x100
	s_addc_u32 s11, s11, 0
	s_cmp_gt_u32 s49, 5
	s_cselect_b32 s49, s49, s52
	s_cbranch_scc0 .LBB0_986
.LBB0_991:
	s_nop 0
	s_and_b64 vcc, exec, s[58:59]
	s_cbranch_vccz .LBB0_993
	s_barrier

.LBB0_1270:
	s_and_b64 s[20:21], s[14:15], s[18:19]
	s_add_i32 s13, s11, 2
	s_and_b64 s[18:19], s[18:19], exec
	s_cselect_b32 s96, 0, s13
	s_and_b64 s[18:19], s[20:21], exec
	s_cselect_b32 s18, s10, s12
	s_mul_hi_i32 s19, s18, 0x2aaaaaab
	s_cselect_b32 s20, s81, s93
	s_lshr_b32 s21, s19, 31
	s_add_i32 s19, s19, s21
	s_mul_i32 s21, s19, 6
	s_sub_i32 s18, s18, s21
	s_cmp_lt_u32 s18, 5
	s_cselect_b32 s21, 1, 2
	s_min_u32 s25, s18, 4
	s_add_i32 s24, s18, 1
	s_add_i32 s25, s25, -1
	s_cmp_lt_i32 s18, 3
	s_cselect_b32 s18, 0, s21
	s_cselect_b32 s21, s24, s25
	s_lshl_b32 s19, s19, 2
	s_or_b32 s18, s18, s19
	s_add_i32 s21, s21, s19
	s_cmp_lt_i32 s20, 4
	s_cselect_b32 s18, s18, s21
	s_lshl_b32 s20, s20, 18
	s_ashr_i32 s19, s18, 31
	s_and_b32 s53, s20, 0xc0000
	s_lshl_b64 s[20:21], s[96:97], 7
	s_or_b32 s96, s96, 1
	s_lshl_b64 s[24:25], s[18:19], 20
	s_lshl_b64 s[18:19], s[96:97], 7
	s_add_u32 s24, s31, s24
	s_addc_u32 s25, s38, s25
	s_add_u32 s53, s24, s53
	s_addc_u32 s72, s25, 0
	s_add_u32 s24, s53, s20
	s_addc_u32 s25, s72, s21
	v_lshl_add_u64 v[218:219], s[24:25], 0, v[196:197]
	s_mov_b32 m0, s41
	ds_read_b128 v[56:59], v244 offset:16384
	ds_read_b128 v[60:63], v245 offset:16384
	ds_read_b128 v[48:51], v244 offset:18432
	ds_read_b128 v[52:55], v245 offset:18432
	ds_read_b128 v[40:43], v244 offset:20480
	ds_read_b128 v[44:47], v245 offset:20480
	ds_read_b128 v[32:35], v244 offset:22528
	ds_read_b128 v[36:39], v245 offset:22528
	global_load_lds_dwordx4 v[218:219], off
	v_lshl_add_u64 v[218:219], s[24:25], 0, v[202:203]
	s_add_u32 s24, s24, 0x20000
	s_mov_b32 m0, s45
	s_addc_u32 s25, s25, 0
	global_load_lds_dwordx4 v[218:219], off
	v_lshl_add_u64 v[218:219], s[24:25], 0, v[196:197]
	s_mov_b32 m0, s48
	s_add_u32 s20, s78, s20
	global_load_lds_dwordx4 v[218:219], off
	v_lshl_add_u64 v[218:219], s[24:25], 0, v[202:203]
	s_mov_b32 m0, s49
	s_addc_u32 s21, s79, s21
	global_load_lds_dwordx4 v[218:219], off
	s_mov_b32 m0, s40
	s_nop 0
	global_load_lds_dwordx4 v208, s[20:21]
	s_mov_b32 m0, s57
	s_nop 0
	global_load_lds_dwordx4 v206, s[20:21]
	s_waitcnt vmcnt(8)
	s_waitcnt lgkmcnt(0)
	s_barrier
	s_setprio 1
	s_waitcnt lgkmcnt(0)
	v_mfma_scale_f32_16x16x128_f8f6f4 v[110:113], v[8:15], v[56:63], v[110:113], v226, v225 op_sel_hi:[0,0,0]
	v_mfma_scale_f32_16x16x128_f8f6f4 v[92:95], v[24:31], v[56:63], v[92:95], v226, v225 op_sel_hi:[0,0,0]
	v_mfma_scale_f32_16x16x128_f8f6f4 v[138:141], v[8:15], v[48:55], v[138:141], v226, v225 op_sel_hi:[0,0,0]
	v_mfma_scale_f32_16x16x128_f8f6f4 v[122:125], v[24:31], v[48:55], v[122:125], v226, v225 op_sel_hi:[0,0,0]
	v_mfma_scale_f32_16x16x128_f8f6f4 v[170:173], v[8:15], v[40:47], v[170:173], v226, v225 op_sel_hi:[0,0,0]
	v_mfma_scale_f32_16x16x128_f8f6f4 v[154:157], v[24:31], v[40:47], v[154:157], v226, v225 op_sel_hi:[0,0,0]
	v_mfma_scale_f32_16x16x128_f8f6f4 v[186:189], v[8:15], v[32:39], v[186:189], v226, v225 op_sel_hi:[0,0,0]
	v_mfma_scale_f32_16x16x128_f8f6f4 v[178:181], v[24:31], v[32:39], v[178:181], v226, v225 op_sel_hi:[0,0,0]
	s_setprio 0
	s_setprio 1
	v_mfma_scale_f32_16x16x128_f8f6f4 v[114:117], v[0:7], v[56:63], v[114:117], v226, v225 op_sel_hi:[0,0,0]
	v_mfma_scale_f32_16x16x128_f8f6f4 v[98:101], v[16:23], v[56:63], v[98:101], v226, v225 op_sel_hi:[0,0,0]
	v_mfma_scale_f32_16x16x128_f8f6f4 v[146:149], v[0:7], v[48:55], v[146:149], v226, v225 op_sel_hi:[0,0,0]
	v_mfma_scale_f32_16x16x128_f8f6f4 v[130:133], v[16:23], v[48:55], v[130:133], v226, v225 op_sel_hi:[0,0,0]
	v_mfma_scale_f32_16x16x128_f8f6f4 v[174:177], v[0:7], v[40:47], v[174:177], v226, v225 op_sel_hi:[0,0,0]
	v_mfma_scale_f32_16x16x128_f8f6f4 v[162:165], v[16:23], v[40:47], v[162:165], v226, v225 op_sel_hi:[0,0,0]
	v_mfma_scale_f32_16x16x128_f8f6f4 v[190:193], v[0:7], v[32:39], v[190:193], v226, v225 op_sel_hi:[0,0,0]
	v_mfma_scale_f32_16x16x128_f8f6f4 v[182:185], v[16:23], v[32:39], v[182:185], v226, v225 op_sel_hi:[0,0,0]
	s_setprio 0
	s_barrier
	s_add_i32 s24, 0, 0x18000
	s_add_i32 s25, 0, 0x1c000
	v_add_u32_e32 v0, s24, v209
	v_add_u32_e32 v4, s24, v239
	v_add_u32_e32 v8, s94, v209
	v_add_u32_e32 v12, s94, v239
	v_add_u32_e32 v16, s25, v209
	v_add_u32_e32 v20, s25, v239
	v_add_u32_e32 v24, s33, v209
	v_add_u32_e32 v28, s33, v239
	ds_read_b128 v[0:3], v0
	ds_read_b128 v[4:7], v4
	ds_read_b128 v[8:11], v8
	ds_read_b128 v[12:15], v12
	ds_read_b128 v[16:19], v16
	ds_read_b128 v[20:23], v20
	ds_read_b128 v[24:27], v24
	ds_read_b128 v[28:31], v28
	s_mov_b32 m0, s58
	v_lshl_add_u64 v[216:217], s[20:21], 0, v[216:217]
	ds_read_b128 v[32:35], v244 offset:32768
	ds_read_b128 v[40:43], v244 offset:34816
	ds_read_b128 v[36:39], v245 offset:32768
	ds_read_b128 v[44:47], v245 offset:34816
	ds_read_b128 v[48:51], v244 offset:36864
	ds_read_b128 v[56:59], v244 offset:38912
	ds_read_b128 v[52:55], v245 offset:36864
	ds_read_b128 v[60:63], v245 offset:38912
	global_load_lds_dwordx4 v[216:217], off
	v_lshl_add_u64 v[214:215], s[20:21], 0, v[214:215]
	s_mov_b32 m0, s59
	s_nop 0
	global_load_lds_dwordx4 v[214:215], off
	s_waitcnt vmcnt(8)
	s_waitcnt lgkmcnt(0)
	s_barrier
	s_setprio 1
	s_waitcnt lgkmcnt(0)
	v_mfma_scale_f32_16x16x128_f8f6f4 v[72:75], v[0:7], v[32:39], v[72:75], v226, v225 op_sel_hi:[0,0,0]
	v_mfma_scale_f32_16x16x128_f8f6f4 v[64:67], v[8:15], v[32:39], v[64:67], v226, v225 op_sel_hi:[0,0,0]
	v_mfma_scale_f32_16x16x128_f8f6f4 v[88:91], v[0:7], v[40:47], v[88:91], v226, v225 op_sel_hi:[0,0,0]
	v_mfma_scale_f32_16x16x128_f8f6f4 v[80:83], v[8:15], v[40:47], v[80:83], v226, v225 op_sel_hi:[0,0,0]
	v_mfma_scale_f32_16x16x128_f8f6f4 v[126:129], v[0:7], v[48:55], v[126:129], v226, v225 op_sel_hi:[0,0,0]
	v_mfma_scale_f32_16x16x128_f8f6f4 v[106:109], v[8:15], v[48:55], v[106:109], v226, v225 op_sel_hi:[0,0,0]
	v_mfma_scale_f32_16x16x128_f8f6f4 v[158:161], v[0:7], v[56:63], v[158:161], v226, v225 op_sel_hi:[0,0,0]
	v_mfma_scale_f32_16x16x128_f8f6f4 v[142:145], v[8:15], v[56:63], v[142:145], v226, v225 op_sel_hi:[0,0,0]
	s_setprio 0
	s_setprio 1
	v_mfma_scale_f32_16x16x128_f8f6f4 v[76:79], v[16:23], v[32:39], v[76:79], v226, v225 op_sel_hi:[0,0,0]
	v_mfma_scale_f32_16x16x128_f8f6f4 v[68:71], v[24:31], v[32:39], v[68:71], v226, v225 op_sel_hi:[0,0,0]
	v_mfma_scale_f32_16x16x128_f8f6f4 v[102:105], v[16:23], v[40:47], v[102:105], v226, v225 op_sel_hi:[0,0,0]
	v_mfma_scale_f32_16x16x128_f8f6f4 v[84:87], v[24:31], v[40:47], v[84:87], v226, v225 op_sel_hi:[0,0,0]
	v_mfma_scale_f32_16x16x128_f8f6f4 v[134:137], v[16:23], v[48:55], v[134:137], v226, v225 op_sel_hi:[0,0,0]
	v_mfma_scale_f32_16x16x128_f8f6f4 v[118:121], v[24:31], v[48:55], v[118:121], v226, v225 op_sel_hi:[0,0,0]
	v_mfma_scale_f32_16x16x128_f8f6f4 v[166:169], v[16:23], v[56:63], v[166:169], v226, v225 op_sel_hi:[0,0,0]
	v_mfma_scale_f32_16x16x128_f8f6f4 v[150:153], v[24:31], v[56:63], v[150:153], v226, v225 op_sel_hi:[0,0,0]
	s_setprio 0
	s_barrier
	s_add_u32 s20, s53, s18
	s_addc_u32 s21, s72, s19
	s_add_i32 s24, s24, s39
	v_lshl_add_u64 v[214:215], s[20:21], 0, v[196:197]
	s_mov_b32 m0, s24
	ds_read_b128 v[32:35], v244 offset:49152
	ds_read_b128 v[40:43], v244 offset:51200
	ds_read_b128 v[36:39], v245 offset:49152
	ds_read_b128 v[44:47], v245 offset:51200
	ds_read_b128 v[48:51], v244 offset:53248
	ds_read_b128 v[56:59], v244 offset:55296
	ds_read_b128 v[52:55], v245 offset:53248
	ds_read_b128 v[60:63], v245 offset:55296
	global_load_lds_dwordx4 v[214:215], off
	s_add_i32 m0, s24, 0x2000
	v_lshl_add_u64 v[214:215], s[20:21], 0, v[202:203]
	s_add_u32 s20, s20, 0x20000
	s_addc_u32 s21, s21, 0
	s_add_i32 s24, s25, s39
	global_load_lds_dwordx4 v[214:215], off
	v_lshl_add_u64 v[214:215], s[20:21], 0, v[196:197]
	s_mov_b32 m0, s24
	s_nop 0
	global_load_lds_dwordx4 v[214:215], off
	s_add_i32 m0, s24, 0x2000
	v_lshl_add_u64 v[214:215], s[20:21], 0, v[202:203]
	s_add_u32 s18, s78, s18
	global_load_lds_dwordx4 v[214:215], off
	s_addc_u32 s19, s79, s19
	s_mov_b32 m0, s60
	s_nop 0
	global_load_lds_dwordx4 v208, s[18:19]
	s_mov_b32 m0, s61
	s_nop 0
	global_load_lds_dwordx4 v206, s[18:19]
	s_waitcnt vmcnt(8)
	s_waitcnt lgkmcnt(0)
	s_barrier
	s_setprio 1
	s_waitcnt lgkmcnt(0)
	v_mfma_scale_f32_16x16x128_f8f6f4 v[110:113], v[0:7], v[32:39], v[110:113], v226, v225 op_sel_hi:[0,0,0]
	v_mfma_scale_f32_16x16x128_f8f6f4 v[92:95], v[8:15], v[32:39], v[92:95], v226, v225 op_sel_hi:[0,0,0]
	v_mfma_scale_f32_16x16x128_f8f6f4 v[138:141], v[0:7], v[40:47], v[138:141], v226, v225 op_sel_hi:[0,0,0]
	v_mfma_scale_f32_16x16x128_f8f6f4 v[122:125], v[8:15], v[40:47], v[122:125], v226, v225 op_sel_hi:[0,0,0]
	v_mfma_scale_f32_16x16x128_f8f6f4 v[170:173], v[0:7], v[48:55], v[170:173], v226, v225 op_sel_hi:[0,0,0]
	v_mfma_scale_f32_16x16x128_f8f6f4 v[154:157], v[8:15], v[48:55], v[154:157], v226, v225 op_sel_hi:[0,0,0]
	v_mfma_scale_f32_16x16x128_f8f6f4 v[186:189], v[0:7], v[56:63], v[186:189], v226, v225 op_sel_hi:[0,0,0]
	v_mfma_scale_f32_16x16x128_f8f6f4 v[178:181], v[8:15], v[56:63], v[178:181], v226, v225 op_sel_hi:[0,0,0]
	s_setprio 0
	s_setprio 1
	v_mfma_scale_f32_16x16x128_f8f6f4 v[114:117], v[16:23], v[32:39], v[114:117], v226, v225 op_sel_hi:[0,0,0]
	v_mfma_scale_f32_16x16x128_f8f6f4 v[98:101], v[24:31], v[32:39], v[98:101], v226, v225 op_sel_hi:[0,0,0]
	v_mfma_scale_f32_16x16x128_f8f6f4 v[146:149], v[16:23], v[40:47], v[146:149], v226, v225 op_sel_hi:[0,0,0]
	v_mfma_scale_f32_16x16x128_f8f6f4 v[130:133], v[24:31], v[40:47], v[130:133], v226, v225 op_sel_hi:[0,0,0]
	v_mfma_scale_f32_16x16x128_f8f6f4 v[174:177], v[16:23], v[48:55], v[174:177], v226, v225 op_sel_hi:[0,0,0]
	v_mfma_scale_f32_16x16x128_f8f6f4 v[162:165], v[24:31], v[48:55], v[162:165], v226, v225 op_sel_hi:[0,0,0]
	v_mfma_scale_f32_16x16x128_f8f6f4 v[190:193], v[16:23], v[56:63], v[190:193], v226, v225 op_sel_hi:[0,0,0]
	v_mfma_scale_f32_16x16x128_f8f6f4 v[182:185], v[24:31], v[56:63], v[182:185], v226, v225 op_sel_hi:[0,0,0]
	s_setprio 0
	s_barrier
	s_add_u32 s16, s16, 0x100
	s_addc_u32 s17, s17, 0
	s_cmp_gt_u32 s11, 5
	s_cselect_b32 s11, s11, s13
	s_cbranch_scc0 .LBB0_1267
.LBB0_1272:
	s_nop 0
	s_and_b64 vcc, exec, s[8:9]
	s_cbranch_vccz .LBB0_1274
	s_barrier
